# split barrier after in-projection, only wave 0 polls memory, other waves wait on an LDS flag
# baseline (speedup 1.0000x reference)
; __global__ void __launch_bounds__(512, 2) hymba_fwd(Args args) {
;     ...
;                 const bool doA = (((hs & 1) == 0) == (wave < 4));
;                 if (doA) { if (ia < nA) { const int a = bx + ia * G; const int blk = a >> 4, h = a & 15;
;                         attn_wave(Qb, Kb, Vb, MIX, h, 256 * blk + wave, vbuf, btab + h * 396, lane); ++ia; } }
.LBB0_214:
	s_and_b32 s0, s83, 1
	v_cmp_ne_u32_e32 vcc, s0, v223
	s_mov_b64 s[6:7], -1
	s_cbranch_vccnz .LBB0_234
	s_cmp_ge_i32 s82, s69
	s_mov_b32 s0, s82
	s_cbranch_scc1 .LBB0_233
	s_cmp_lg_u32 s98, 0
	s_cbranch_scc1 .Lp2gb_passed
	s_waitcnt vmcnt(0) lgkmcnt(0)
	s_mov_b32 s99, 0
	s_cmp_lg_u32 s92, 0
	s_cbranch_scc1 .Lp2gb_follow
	v_mov_b32_e32 v21, 0x22604
	ds_read_b32 v233, v21
	v_mov_b32_e32 v21, 0x3000
	s_waitcnt lgkmcnt(0)
	v_mul_u32_u24_e32 v233, 2, v233

; __global__ void __launch_bounds__(512, 2) hymba_fwd(Args args) {
;     ...
;                 const bool doA = (((hs & 1) == 0) == (wave < 4));
;                 if (doA) { if (ia < nA) { const int a = bx + ia * G; const int blk = a >> 4, h = a & 15;
;                         attn_wave(Qb, Kb, Vb, MIX, h, 256 * blk + wave, vbuf, btab + h * 396, lane); ++ia; } }
.Lp2gb_lead_done:
	buffer_inv sc1
	v_mov_b32_e32 v21, 0x22610
	v_mov_b32_e32 v22, 1
	ds_write_b32 v21, v22
	s_waitcnt vmcnt(0) lgkmcnt(0)
	s_branch .Lp2gb_done
.Lp2gb_follow:
	v_mov_b32_e32 v21, 0x22610
.Lp2gb_fspin:
	ds_read_b32 v22, v21
	s_waitcnt lgkmcnt(0)
	v_cmp_ne_u32_e32 vcc, 0, v22
	s_cbranch_vccnz .Lp2gb_fdone
	s_sleep 1
	s_add_i32 s99, s99, 1
	s_cmp_lt_u32 s99, 0x80000
	s_cbranch_scc1 .Lp2gb_fspin

; __global__ void __launch_bounds__(512, 2) hymba_fwd(Args args) {
;     ...
;                 const bool doA = (((hs & 1) == 0) == (wave < 4));
;                 if (doA) { if (ia < nA) { const int a = bx + ia * G; const int blk = a >> 4, h = a & 15;
;                         attn_wave(Qb, Kb, Vb, MIX, h, 256 * blk + wave, vbuf, btab + h * 396, lane); ++ia; } }
.Lp2gb_done:
	s_mov_b32 s98, 1
